# P5 final epilogue: the 16 gate loads issued up front into free registers, counted vmcnt(15) per block instead of vmcnt(0) behind each store
# baseline (speedup 1.0000x reference)
; __device__ __forceinline__ unsigned cvt4_fp8(float a, float b, float c, float d) { int w = 0; w = __builtin_amdgcn_cvt_pk_fp8_f32(a, b, w, false); w = __builtin_amdgcn_cvt_pk_fp8_f32(c, d, w, true); return (unsigned)w; }
; __device__ __forceinline__ float sigmoidf_(float x) { return __builtin_amdgcn_rcpf(1.0f + __expf(-x)); }
; __device__ __forceinline__ void unpack8(u32x4 w, f32x4& a, f32x4& b) { a = (f32x4){bflo(w.x), bfhi(w.x), bflo(w.y), bfhi(w.y)}; b = (f32x4){bflo(w.z), bfhi(w.z), bflo(w.w), bfhi(w.w)}; }
;     __device__ __forceinline__ void operator()(const Acc& acc, const Unit& u, int wr, int wc, int fr, int fq) const {
;         const int row0 = u.row0 + wr * 64 + fr, col0 = u.col0 + wc * 32 + 8 * fq;
; #pragma unroll
;         for (int ai = 0; ai < 2; ++ai)
; #pragma unroll
;             for (int m = 0; m < 4; ++m) { const int row = row0 + ai * HALF + m * 16;
; #pragma unroll
;                 for (int bj = 0; bj < 2; ++bj) { const int col = col0 + bj * HALF;
;                     f32x4 b0, b1; unpack8(*(const u32x4*)(GB + (size_t)row * ldg + col), b0, b1);
;                     f32x4 v0 = acc[ai][bj][m][0], v1 = acc[ai][bj][m][1];
; #pragma unroll
;                     for (int j = 0; j < 4; ++j) { v0[j] *= 16.0f * sigmoidf_(b0[j]); v1[j] *= 16.0f * sigmoidf_(b1[j]); }
;                     u32x2 w; w.x = cvt4_fp8(v0[0], v0[1], v0[2], v0[3]); w.y = cvt4_fp8(v1[0], v1[1], v1[2], v1[3]); *(u32x2*)(O + (size_t)row * ldc + col) = w; } }
;     }
.LBB0_1855:
	s_nop 15
	s_nop 15
	v_mbcnt_lo_u32_b32 v2, -1, 0
	v_mbcnt_hi_u32_b32 v2, -1, v2
	v_mov_b64_e32 v[4:5], s[8:9]
	v_and_b32_e32 v3, 15, v2
	v_ashrrev_i32_e32 v2, 1, v2
	v_and_b32_e32 v2, -8, v2
	v_add_u32_e32 v2, s77, v2
	v_add_u32_e32 v8, s78, v3
	v_ashrrev_i32_e32 v3, 31, v2
	v_mad_i64_i32 v[12:13], s[26:27], v8, s73, v[4:5]
	v_lshlrev_b64 v[6:7], 1, v[2:3]
	v_lshl_add_u64 v[12:13], v[12:13], 0, v[6:7]
	v_mad_i64_i32 v[248:249], s[26:27], v8, s73, v[4:5]
	v_lshl_add_u64 v[248:249], v[248:249], 0, v[6:7]
	global_load_dwordx4 v[182:185], v[248:249], off
	global_load_dwordx4 v[186:189], v[248:249], off offset:256
	v_add_u32_e32 v250, 16, v8
	v_mad_i64_i32 v[248:249], s[26:27], v250, s73, v[4:5]
	v_lshl_add_u64 v[248:249], v[248:249], 0, v[6:7]
	global_load_dwordx4 v[190:193], v[248:249], off
	global_load_dwordx4 v[194:197], v[248:249], off offset:256
	v_add_u32_e32 v250, 32, v8
	v_mad_i64_i32 v[248:249], s[26:27], v250, s73, v[4:5]
	v_lshl_add_u64 v[248:249], v[248:249], 0, v[6:7]
	global_load_dwordx4 v[200:203], v[248:249], off
	global_load_dwordx4 v[204:207], v[248:249], off offset:256
	v_add_u32_e32 v250, 48, v8
	v_mad_i64_i32 v[248:249], s[26:27], v250, s73, v[4:5]
	v_lshl_add_u64 v[248:249], v[248:249], 0, v[6:7]
	global_load_dwordx4 v[208:211], v[248:249], off
	global_load_dwordx4 v[212:215], v[248:249], off offset:256
	v_add_u32_e32 v250, 128, v8
	v_mad_i64_i32 v[248:249], s[26:27], v250, s73, v[4:5]
	v_lshl_add_u64 v[248:249], v[248:249], 0, v[6:7]
	global_load_dwordx4 v[216:219], v[248:249], off
	global_load_dwordx4 v[220:223], v[248:249], off offset:256
	v_add_u32_e32 v250, 144, v8
	v_mad_i64_i32 v[248:249], s[26:27], v250, s73, v[4:5]
	v_lshl_add_u64 v[248:249], v[248:249], 0, v[6:7]
	global_load_dwordx4 v[224:227], v[248:249], off
	global_load_dwordx4 v[228:231], v[248:249], off offset:256
	v_add_u32_e32 v250, 160, v8
	v_mad_i64_i32 v[248:249], s[26:27], v250, s73, v[4:5]
	v_lshl_add_u64 v[248:249], v[248:249], 0, v[6:7]
	global_load_dwordx4 v[232:235], v[248:249], off
	global_load_dwordx4 v[236:239], v[248:249], off offset:256
	v_add_u32_e32 v250, 176, v8
	v_mad_i64_i32 v[248:249], s[26:27], v250, s73, v[4:5]
	v_lshl_add_u64 v[248:249], v[248:249], 0, v[6:7]
	global_load_dwordx4 v[240:243], v[248:249], off
	global_load_dwordx4 v[244:247], v[248:249], off offset:256
	v_mov_b32_e32 v156, 0
	v_mov_b32_e32 v157, 0
	v_ashrrev_i32_e32 v9, 31, v8
	s_andn2_b64 vcc, exec, s[12:13]
	s_mov_b64 s[12:13], -1
	s_waitcnt vmcnt(15)
	v_mov_b32_e32 v152, v182
	v_mov_b32_e32 v153, v183
	v_mov_b32_e32 v154, v184
	v_mov_b32_e32 v155, v185
	v_lshlrev_b32_e32 v11, 16, v152
	v_and_b32_e32 v151, 0xffff0000, v152
	v_lshlrev_b32_e32 v158, 16, v154
	v_and_b32_e32 v154, 0xffff0000, v154
	v_mul_f32_e32 v11, 0xbfb8aa3b, v11
	v_mul_f32_e32 v158, 0xbfb8aa3b, v158
	v_mul_f32_e32 v151, 0xbfb8aa3b, v151
	v_mul_f32_e32 v154, 0xbfb8aa3b, v154
	v_exp_f32_e32 v11, v11
	v_exp_f32_e32 v158, v158
	v_exp_f32_e32 v151, v151
	v_exp_f32_e32 v154, v154
	v_lshlrev_b32_e32 v152, 16, v153
	v_and_b32_e32 v153, 0xffff0000, v153
	v_lshlrev_b32_e32 v159, 16, v155
	v_and_b32_e32 v155, 0xffff0000, v155
	v_mul_f32_e32 v152, 0xbfb8aa3b, v152
	v_mul_f32_e32 v159, 0xbfb8aa3b, v159
	v_mul_f32_e32 v153, 0xbfb8aa3b, v153
	v_mul_f32_e32 v155, 0xbfb8aa3b, v155
	v_exp_f32_e32 v152, v152
	v_exp_f32_e32 v159, v159
	v_exp_f32_e32 v153, v153
	v_exp_f32_e32 v155, v155
	v_add_f32_e32 v11, 1.0, v11
	v_add_f32_e32 v158, 1.0, v158
	v_add_f32_e32 v151, 1.0, v151
	v_add_f32_e32 v154, 1.0, v154
	v_rcp_f32_e32 v11, v11
	v_rcp_f32_e32 v158, v158
	v_rcp_f32_e32 v151, v151
	v_rcp_f32_e32 v154, v154
	v_add_f32_e32 v152, 1.0, v152
	v_add_f32_e32 v159, 1.0, v159
	v_add_f32_e32 v153, 1.0, v153
	v_add_f32_e32 v155, 1.0, v155
	v_rcp_f32_e32 v152, v152
	v_rcp_f32_e32 v159, v159
	v_rcp_f32_e32 v153, v153
	v_rcp_f32_e32 v155, v155
	v_mul_f32_e32 v11, 0x41800000, v11
	v_mul_f32_e32 v158, 0x41800000, v158
	v_mul_f32_e32 v151, 0x41800000, v151
	v_mul_f32_e32 v154, 0x41800000, v154
	v_mul_f32_e32 v11, v138, v11
	v_mul_f32_e32 v134, v134, v158
	v_mul_f32_e32 v138, v139, v151
	v_mul_f32_e32 v135, v135, v154
	v_cvt_pk_fp8_f32 v156, v11, v138
	v_cvt_pk_fp8_f32 v157, v134, v135
	v_mul_f32_e32 v152, 0x41800000, v152
	v_mul_f32_e32 v159, 0x41800000, v159
	v_mul_f32_e32 v153, 0x41800000, v153
	v_mul_f32_e32 v155, 0x41800000, v155
	v_mul_f32_e32 v139, v140, v152
	v_mul_f32_e32 v136, v136, v159
	v_mul_f32_e32 v11, v141, v153
	v_mul_f32_e32 v134, v137, v155
	v_cvt_pk_fp8_f32 v156, v139, v11 op_sel:[0,0,1]
	v_cvt_pk_fp8_f32 v157, v136, v134 op_sel:[0,0,1]
	v_lshlrev_b64 v[134:135], 11, v[8:9]
	v_lshl_add_u64 v[134:135], s[36:37], 0, v[134:135]
	v_lshl_add_u64 v[138:139], v[134:135], 0, v[2:3]
	global_store_dwordx2 v[138:139], v[156:157], off
	v_mov_b32_e32 v12, 0
	v_mov_b32_e32 v13, 0
	v_add_u32_e32 v140, 16, v8
	s_waitcnt vmcnt(15)
; __device__ __forceinline__ unsigned cvt4_fp8(float a, float b, float c, float d) { int w = 0; w = __builtin_amdgcn_cvt_pk_fp8_f32(a, b, w, false); w = __builtin_amdgcn_cvt_pk_fp8_f32(c, d, w, true); return (unsigned)w; }
; __device__ __forceinline__ float sigmoidf_(float x) { return __builtin_amdgcn_rcpf(1.0f + __expf(-x)); }
; __device__ __forceinline__ void unpack8(u32x4 w, f32x4& a, f32x4& b) { a = (f32x4){bflo(w.x), bfhi(w.x), bflo(w.y), bfhi(w.y)}; b = (f32x4){bflo(w.z), bfhi(w.z), bflo(w.w), bfhi(w.w)}; }
;     __device__ __forceinline__ void operator()(const Acc& acc, const Unit& u, int wr, int wc, int fr, int fq) const {
;     ...
;                 for (int bj = 0; bj < 2; ++bj) { const int col = col0 + bj * HALF;
;                     f32x4 b0, b1; unpack8(*(const u32x4*)(GB + (size_t)row * ldg + col), b0, b1);
;                     f32x4 v0 = acc[ai][bj][m][0], v1 = acc[ai][bj][m][1];
; #pragma unroll
;                     for (int j = 0; j < 4; ++j) { v0[j] *= 16.0f * sigmoidf_(b0[j]); v1[j] *= 16.0f * sigmoidf_(b1[j]); }
;                     u32x2 w; w.x = cvt4_fp8(v0[0], v0[1], v0[2], v0[3]); w.y = cvt4_fp8(v1[0], v1[1], v1[2], v1[3]); *(u32x2*)(O + (size_t)row * ldc + col) = w; } }
	v_mov_b32_e32 v134, v186
	v_mov_b32_e32 v135, v187
	v_mov_b32_e32 v136, v188
	v_mov_b32_e32 v137, v189
	v_lshlrev_b32_e32 v9, 16, v134
	v_and_b32_e32 v11, 0xffff0000, v134
	v_lshlrev_b32_e32 v141, 16, v136
	v_and_b32_e32 v136, 0xffff0000, v136
	v_mul_f32_e32 v9, 0xbfb8aa3b, v9
	v_mul_f32_e32 v141, 0xbfb8aa3b, v141
	v_mul_f32_e32 v11, 0xbfb8aa3b, v11
	v_mul_f32_e32 v136, 0xbfb8aa3b, v136
	v_exp_f32_e32 v9, v9
	v_exp_f32_e32 v141, v141
	v_exp_f32_e32 v11, v11
	v_exp_f32_e32 v136, v136
	v_lshlrev_b32_e32 v134, 16, v135
	v_and_b32_e32 v135, 0xffff0000, v135
	v_lshlrev_b32_e32 v151, 16, v137
	v_and_b32_e32 v137, 0xffff0000, v137
	v_mul_f32_e32 v134, 0xbfb8aa3b, v134
	v_mul_f32_e32 v151, 0xbfb8aa3b, v151
	v_mul_f32_e32 v135, 0xbfb8aa3b, v135
	v_mul_f32_e32 v137, 0xbfb8aa3b, v137
	v_exp_f32_e32 v134, v134
	v_exp_f32_e32 v151, v151
	v_exp_f32_e32 v135, v135
	v_exp_f32_e32 v137, v137
	v_add_f32_e32 v9, 1.0, v9
	v_add_f32_e32 v141, 1.0, v141
	v_add_f32_e32 v11, 1.0, v11
	v_add_f32_e32 v136, 1.0, v136
	v_rcp_f32_e32 v9, v9
	v_rcp_f32_e32 v141, v141
	v_rcp_f32_e32 v11, v11
	v_rcp_f32_e32 v136, v136
	v_add_f32_e32 v134, 1.0, v134
	v_add_f32_e32 v151, 1.0, v151
	v_add_f32_e32 v135, 1.0, v135
	v_add_f32_e32 v137, 1.0, v137
	v_rcp_f32_e32 v134, v134
	v_rcp_f32_e32 v151, v151
	v_rcp_f32_e32 v135, v135
	v_rcp_f32_e32 v137, v137
	v_mul_f32_e32 v9, 0x41800000, v9
	v_mul_f32_e32 v141, 0x41800000, v141
	v_mul_f32_e32 v11, 0x41800000, v11
	v_mul_f32_e32 v136, 0x41800000, v136
	v_mul_f32_e32 v9, v130, v9
	v_mul_f32_e32 v126, v126, v141
	v_mul_f32_e32 v11, v131, v11
	v_mul_f32_e32 v127, v127, v136
	v_cvt_pk_fp8_f32 v12, v9, v11
	v_cvt_pk_fp8_f32 v13, v126, v127
	v_mul_f32_e32 v134, 0x41800000, v134
	v_mul_f32_e32 v151, 0x41800000, v151
	v_mul_f32_e32 v135, 0x41800000, v135
	v_mul_f32_e32 v137, 0x41800000, v137
	v_mul_f32_e32 v130, v132, v134
	v_mul_f32_e32 v128, v128, v151
	v_mul_f32_e32 v9, v133, v135
	v_mul_f32_e32 v11, v129, v137
	v_cvt_pk_fp8_f32 v12, v130, v9 op_sel:[0,0,1]
	v_cvt_pk_fp8_f32 v13, v128, v11 op_sel:[0,0,1]
	v_mad_i64_i32 v[126:127], s[26:27], v140, s73, v[4:5]
	v_lshl_add_u64 v[130:131], v[126:127], 0, v[6:7]
	global_store_dwordx2 v[138:139], v[12:13], off offset:128
	v_mov_b32_e32 v12, 0
	v_mov_b32_e32 v13, 0
	v_ashrrev_i32_e32 v141, 31, v140
	s_waitcnt vmcnt(15)
	v_mov_b32_e32 v126, v190
	v_mov_b32_e32 v127, v191
	v_mov_b32_e32 v128, v192
	v_mov_b32_e32 v129, v193
	v_lshlrev_b32_e32 v9, 16, v126
	v_and_b32_e32 v11, 0xffff0000, v126
	v_lshlrev_b32_e32 v132, 16, v128
	v_and_b32_e32 v128, 0xffff0000, v128
	v_mul_f32_e32 v9, 0xbfb8aa3b, v9
	v_mul_f32_e32 v132, 0xbfb8aa3b, v132
	v_mul_f32_e32 v11, 0xbfb8aa3b, v11
	v_mul_f32_e32 v128, 0xbfb8aa3b, v128
	v_exp_f32_e32 v9, v9
	v_exp_f32_e32 v132, v132
	v_exp_f32_e32 v11, v11
	v_exp_f32_e32 v128, v128
	v_lshlrev_b32_e32 v126, 16, v127
	v_and_b32_e32 v127, 0xffff0000, v127
	v_lshlrev_b32_e32 v133, 16, v129
	v_and_b32_e32 v129, 0xffff0000, v129
	v_mul_f32_e32 v126, 0xbfb8aa3b, v126
	v_mul_f32_e32 v133, 0xbfb8aa3b, v133
	v_mul_f32_e32 v127, 0xbfb8aa3b, v127
	v_mul_f32_e32 v129, 0xbfb8aa3b, v129
	v_exp_f32_e32 v126, v126
	v_exp_f32_e32 v133, v133
	v_exp_f32_e32 v127, v127
	v_exp_f32_e32 v129, v129
	v_add_f32_e32 v9, 1.0, v9
	v_add_f32_e32 v132, 1.0, v132
	v_add_f32_e32 v11, 1.0, v11
	v_add_f32_e32 v128, 1.0, v128
	v_rcp_f32_e32 v9, v9
	v_rcp_f32_e32 v132, v132
	v_rcp_f32_e32 v11, v11
	v_rcp_f32_e32 v128, v128
	v_add_f32_e32 v126, 1.0, v126
	v_add_f32_e32 v133, 1.0, v133
	v_add_f32_e32 v127, 1.0, v127
	v_add_f32_e32 v129, 1.0, v129
	v_rcp_f32_e32 v126, v126
	v_rcp_f32_e32 v133, v133
	v_rcp_f32_e32 v127, v127
	v_rcp_f32_e32 v129, v129
	v_mul_f32_e32 v9, 0x41800000, v9
	v_mul_f32_e32 v132, 0x41800000, v132
	v_mul_f32_e32 v11, 0x41800000, v11
	v_mul_f32_e32 v128, 0x41800000, v128
	v_mul_f32_e32 v9, v122, v9
	v_mul_f32_e32 v118, v118, v132
	v_mul_f32_e32 v11, v123, v11
	v_mul_f32_e32 v119, v119, v128
	v_cvt_pk_fp8_f32 v12, v9, v11
	v_cvt_pk_fp8_f32 v13, v118, v119
	v_mul_f32_e32 v126, 0x41800000, v126
	v_mul_f32_e32 v133, 0x41800000, v133
	v_mul_f32_e32 v127, 0x41800000, v127
	v_mul_f32_e32 v129, 0x41800000, v129
	v_mul_f32_e32 v122, v124, v126
	v_mul_f32_e32 v120, v120, v133
	v_mul_f32_e32 v9, v125, v127
	v_mul_f32_e32 v11, v121, v129
	v_cvt_pk_fp8_f32 v12, v122, v9 op_sel:[0,0,1]
	v_cvt_pk_fp8_f32 v13, v120, v11 op_sel:[0,0,1]
	v_lshlrev_b64 v[118:119], 11, v[140:141]
	v_lshl_add_u64 v[118:119], s[36:37], 0, v[118:119]
	v_lshl_add_u64 v[122:123], v[118:119], 0, v[2:3]
	global_store_dwordx2 v[122:123], v[12:13], off
	v_mov_b32_e32 v12, 0
	v_mov_b32_e32 v13, 0
	v_add_u32_e32 v124, 32, v8
	s_waitcnt vmcnt(15)
; __device__ __forceinline__ unsigned cvt4_fp8(float a, float b, float c, float d) { int w = 0; w = __builtin_amdgcn_cvt_pk_fp8_f32(a, b, w, false); w = __builtin_amdgcn_cvt_pk_fp8_f32(c, d, w, true); return (unsigned)w; }
; __device__ __forceinline__ float sigmoidf_(float x) { return __builtin_amdgcn_rcpf(1.0f + __expf(-x)); }
; __device__ __forceinline__ void unpack8(u32x4 w, f32x4& a, f32x4& b) { a = (f32x4){bflo(w.x), bfhi(w.x), bflo(w.y), bfhi(w.y)}; b = (f32x4){bflo(w.z), bfhi(w.z), bflo(w.w), bfhi(w.w)}; }
;     __device__ __forceinline__ void operator()(const Acc& acc, const Unit& u, int wr, int wc, int fr, int fq) const {
;     ...
;                 for (int bj = 0; bj < 2; ++bj) { const int col = col0 + bj * HALF;
;                     f32x4 b0, b1; unpack8(*(const u32x4*)(GB + (size_t)row * ldg + col), b0, b1);
;                     f32x4 v0 = acc[ai][bj][m][0], v1 = acc[ai][bj][m][1];
; #pragma unroll
;                     for (int j = 0; j < 4; ++j) { v0[j] *= 16.0f * sigmoidf_(b0[j]); v1[j] *= 16.0f * sigmoidf_(b1[j]); }
;                     u32x2 w; w.x = cvt4_fp8(v0[0], v0[1], v0[2], v0[3]); w.y = cvt4_fp8(v1[0], v1[1], v1[2], v1[3]); *(u32x2*)(O + (size_t)row * ldc + col) = w; } }
	v_mov_b32_e32 v118, v194
	v_mov_b32_e32 v119, v195
	v_mov_b32_e32 v120, v196
	v_mov_b32_e32 v121, v197
	v_lshlrev_b32_e32 v9, 16, v118
	v_and_b32_e32 v11, 0xffff0000, v118
	v_lshlrev_b32_e32 v125, 16, v120
	v_and_b32_e32 v120, 0xffff0000, v120
	v_mul_f32_e32 v9, 0xbfb8aa3b, v9
	v_mul_f32_e32 v125, 0xbfb8aa3b, v125
	v_mul_f32_e32 v11, 0xbfb8aa3b, v11
	v_mul_f32_e32 v120, 0xbfb8aa3b, v120
	v_exp_f32_e32 v9, v9
	v_exp_f32_e32 v125, v125
	v_exp_f32_e32 v11, v11
	v_exp_f32_e32 v120, v120
	v_lshlrev_b32_e32 v118, 16, v119
	v_and_b32_e32 v119, 0xffff0000, v119
	v_lshlrev_b32_e32 v126, 16, v121
	v_and_b32_e32 v121, 0xffff0000, v121
	v_mul_f32_e32 v118, 0xbfb8aa3b, v118
	v_mul_f32_e32 v126, 0xbfb8aa3b, v126
	v_mul_f32_e32 v119, 0xbfb8aa3b, v119
	v_mul_f32_e32 v121, 0xbfb8aa3b, v121
	v_exp_f32_e32 v118, v118
	v_exp_f32_e32 v126, v126
	v_exp_f32_e32 v119, v119
	v_exp_f32_e32 v121, v121
	v_add_f32_e32 v9, 1.0, v9
	v_add_f32_e32 v125, 1.0, v125
	v_add_f32_e32 v11, 1.0, v11
	v_add_f32_e32 v120, 1.0, v120
	v_rcp_f32_e32 v9, v9
	v_rcp_f32_e32 v125, v125
	v_rcp_f32_e32 v11, v11
	v_rcp_f32_e32 v120, v120
	v_add_f32_e32 v118, 1.0, v118
	v_add_f32_e32 v126, 1.0, v126
	v_add_f32_e32 v119, 1.0, v119
	v_add_f32_e32 v121, 1.0, v121
	v_rcp_f32_e32 v118, v118
	v_rcp_f32_e32 v126, v126
	v_rcp_f32_e32 v119, v119
	v_rcp_f32_e32 v121, v121
	v_mul_f32_e32 v9, 0x41800000, v9
	v_mul_f32_e32 v125, 0x41800000, v125
	v_mul_f32_e32 v11, 0x41800000, v11
	v_mul_f32_e32 v120, 0x41800000, v120
	v_mul_f32_e32 v9, v114, v9
	v_mul_f32_e32 v110, v110, v125
	v_mul_f32_e32 v11, v115, v11
	v_mul_f32_e32 v111, v111, v120
	v_cvt_pk_fp8_f32 v12, v9, v11
	v_cvt_pk_fp8_f32 v13, v110, v111
	v_mul_f32_e32 v118, 0x41800000, v118
	v_mul_f32_e32 v126, 0x41800000, v126
	v_mul_f32_e32 v119, 0x41800000, v119
	v_mul_f32_e32 v121, 0x41800000, v121
	v_mul_f32_e32 v114, v116, v118
	v_mul_f32_e32 v112, v112, v126
	v_mul_f32_e32 v9, v117, v119
	v_mul_f32_e32 v11, v113, v121
	v_cvt_pk_fp8_f32 v12, v114, v9 op_sel:[0,0,1]
	v_cvt_pk_fp8_f32 v13, v112, v11 op_sel:[0,0,1]
	v_mad_i64_i32 v[110:111], s[26:27], v124, s73, v[4:5]
	v_lshl_add_u64 v[114:115], v[110:111], 0, v[6:7]
	global_store_dwordx2 v[122:123], v[12:13], off offset:128
	v_mov_b32_e32 v12, 0
	v_mov_b32_e32 v13, 0
	v_ashrrev_i32_e32 v125, 31, v124
	s_waitcnt vmcnt(15)
	v_mov_b32_e32 v110, v200
	v_mov_b32_e32 v111, v201
	v_mov_b32_e32 v112, v202
	v_mov_b32_e32 v113, v203
	v_lshlrev_b32_e32 v9, 16, v110
	v_and_b32_e32 v11, 0xffff0000, v110
	v_lshlrev_b32_e32 v116, 16, v112
	v_and_b32_e32 v112, 0xffff0000, v112
	v_mul_f32_e32 v9, 0xbfb8aa3b, v9
	v_mul_f32_e32 v116, 0xbfb8aa3b, v116
	v_mul_f32_e32 v11, 0xbfb8aa3b, v11
	v_mul_f32_e32 v112, 0xbfb8aa3b, v112
	v_exp_f32_e32 v9, v9
	v_exp_f32_e32 v116, v116
	v_exp_f32_e32 v11, v11
	v_exp_f32_e32 v112, v112
	v_lshlrev_b32_e32 v110, 16, v111
	v_and_b32_e32 v111, 0xffff0000, v111
	v_lshlrev_b32_e32 v117, 16, v113
	v_and_b32_e32 v113, 0xffff0000, v113
	v_mul_f32_e32 v110, 0xbfb8aa3b, v110
	v_mul_f32_e32 v117, 0xbfb8aa3b, v117
	v_mul_f32_e32 v111, 0xbfb8aa3b, v111
	v_mul_f32_e32 v113, 0xbfb8aa3b, v113
	v_exp_f32_e32 v110, v110
	v_exp_f32_e32 v117, v117
	v_exp_f32_e32 v111, v111
	v_exp_f32_e32 v113, v113
	v_add_f32_e32 v9, 1.0, v9
	v_add_f32_e32 v116, 1.0, v116
	v_add_f32_e32 v11, 1.0, v11
	v_add_f32_e32 v112, 1.0, v112
	v_rcp_f32_e32 v9, v9
	v_rcp_f32_e32 v116, v116
	v_rcp_f32_e32 v11, v11
	v_rcp_f32_e32 v112, v112
	v_add_f32_e32 v110, 1.0, v110
	v_add_f32_e32 v117, 1.0, v117
	v_add_f32_e32 v111, 1.0, v111
	v_add_f32_e32 v113, 1.0, v113
	v_rcp_f32_e32 v110, v110
	v_rcp_f32_e32 v117, v117
	v_rcp_f32_e32 v111, v111
	v_rcp_f32_e32 v113, v113
	v_mul_f32_e32 v9, 0x41800000, v9
	v_mul_f32_e32 v116, 0x41800000, v116
	v_mul_f32_e32 v11, 0x41800000, v11
	v_mul_f32_e32 v112, 0x41800000, v112
	v_mul_f32_e32 v9, v106, v9
	v_mul_f32_e32 v102, v102, v116
	v_mul_f32_e32 v11, v107, v11
	v_mul_f32_e32 v103, v103, v112
	v_cvt_pk_fp8_f32 v12, v9, v11
	v_cvt_pk_fp8_f32 v13, v102, v103
	v_mul_f32_e32 v110, 0x41800000, v110
	v_mul_f32_e32 v117, 0x41800000, v117
	v_mul_f32_e32 v111, 0x41800000, v111
	v_mul_f32_e32 v113, 0x41800000, v113
	v_mul_f32_e32 v106, v108, v110
	v_mul_f32_e32 v104, v104, v117
	v_mul_f32_e32 v9, v109, v111
	v_mul_f32_e32 v11, v105, v113
	v_cvt_pk_fp8_f32 v12, v106, v9 op_sel:[0,0,1]
	v_cvt_pk_fp8_f32 v13, v104, v11 op_sel:[0,0,1]
	v_lshlrev_b64 v[102:103], 11, v[124:125]
	v_lshl_add_u64 v[102:103], s[36:37], 0, v[102:103]
	v_lshl_add_u64 v[106:107], v[102:103], 0, v[2:3]
	global_store_dwordx2 v[106:107], v[12:13], off
	v_mov_b32_e32 v12, 0
	v_mov_b32_e32 v13, 0
	v_add_u32_e32 v108, 48, v8
	s_waitcnt vmcnt(15)
; __device__ __forceinline__ unsigned cvt4_fp8(float a, float b, float c, float d) { int w = 0; w = __builtin_amdgcn_cvt_pk_fp8_f32(a, b, w, false); w = __builtin_amdgcn_cvt_pk_fp8_f32(c, d, w, true); return (unsigned)w; }
; __device__ __forceinline__ float sigmoidf_(float x) { return __builtin_amdgcn_rcpf(1.0f + __expf(-x)); }
; __device__ __forceinline__ void unpack8(u32x4 w, f32x4& a, f32x4& b) { a = (f32x4){bflo(w.x), bfhi(w.x), bflo(w.y), bfhi(w.y)}; b = (f32x4){bflo(w.z), bfhi(w.z), bflo(w.w), bfhi(w.w)}; }
;     __device__ __forceinline__ void operator()(const Acc& acc, const Unit& u, int wr, int wc, int fr, int fq) const {
;     ...
;                 for (int bj = 0; bj < 2; ++bj) { const int col = col0 + bj * HALF;
;                     f32x4 b0, b1; unpack8(*(const u32x4*)(GB + (size_t)row * ldg + col), b0, b1);
;                     f32x4 v0 = acc[ai][bj][m][0], v1 = acc[ai][bj][m][1];
; #pragma unroll
;                     for (int j = 0; j < 4; ++j) { v0[j] *= 16.0f * sigmoidf_(b0[j]); v1[j] *= 16.0f * sigmoidf_(b1[j]); }
;                     u32x2 w; w.x = cvt4_fp8(v0[0], v0[1], v0[2], v0[3]); w.y = cvt4_fp8(v1[0], v1[1], v1[2], v1[3]); *(u32x2*)(O + (size_t)row * ldc + col) = w; } }
	v_mov_b32_e32 v102, v204
	v_mov_b32_e32 v103, v205
	v_mov_b32_e32 v104, v206
	v_mov_b32_e32 v105, v207
	v_lshlrev_b32_e32 v9, 16, v102
	v_and_b32_e32 v11, 0xffff0000, v102
	v_lshlrev_b32_e32 v109, 16, v104
	v_and_b32_e32 v104, 0xffff0000, v104
	v_mul_f32_e32 v9, 0xbfb8aa3b, v9
	v_mul_f32_e32 v109, 0xbfb8aa3b, v109
	v_mul_f32_e32 v11, 0xbfb8aa3b, v11
	v_mul_f32_e32 v104, 0xbfb8aa3b, v104
	v_exp_f32_e32 v9, v9
	v_exp_f32_e32 v109, v109
	v_exp_f32_e32 v11, v11
	v_exp_f32_e32 v104, v104
	v_lshlrev_b32_e32 v102, 16, v103
	v_and_b32_e32 v103, 0xffff0000, v103
	v_lshlrev_b32_e32 v110, 16, v105
	v_and_b32_e32 v105, 0xffff0000, v105
	v_mul_f32_e32 v102, 0xbfb8aa3b, v102
	v_mul_f32_e32 v110, 0xbfb8aa3b, v110
	v_mul_f32_e32 v103, 0xbfb8aa3b, v103
	v_mul_f32_e32 v105, 0xbfb8aa3b, v105
	v_exp_f32_e32 v102, v102
	v_exp_f32_e32 v110, v110
	v_exp_f32_e32 v103, v103
	v_exp_f32_e32 v105, v105
	v_add_f32_e32 v9, 1.0, v9
	v_add_f32_e32 v109, 1.0, v109
	v_add_f32_e32 v11, 1.0, v11
	v_add_f32_e32 v104, 1.0, v104
	v_rcp_f32_e32 v9, v9
	v_rcp_f32_e32 v109, v109
	v_rcp_f32_e32 v11, v11
	v_rcp_f32_e32 v104, v104
	v_add_f32_e32 v102, 1.0, v102
	v_add_f32_e32 v110, 1.0, v110
	v_add_f32_e32 v103, 1.0, v103
	v_add_f32_e32 v105, 1.0, v105
	v_rcp_f32_e32 v102, v102
	v_rcp_f32_e32 v110, v110
	v_rcp_f32_e32 v103, v103
	v_rcp_f32_e32 v105, v105
	v_mul_f32_e32 v9, 0x41800000, v9
	v_mul_f32_e32 v109, 0x41800000, v109
	v_mul_f32_e32 v11, 0x41800000, v11
	v_mul_f32_e32 v104, 0x41800000, v104
	v_mul_f32_e32 v9, v98, v9
	v_mul_f32_e32 v94, v94, v109
	v_mul_f32_e32 v11, v99, v11
	v_mul_f32_e32 v95, v95, v104
	v_cvt_pk_fp8_f32 v12, v9, v11
	v_cvt_pk_fp8_f32 v13, v94, v95
	v_mul_f32_e32 v102, 0x41800000, v102
	v_mul_f32_e32 v110, 0x41800000, v110
	v_mul_f32_e32 v103, 0x41800000, v103
	v_mul_f32_e32 v105, 0x41800000, v105
	v_mul_f32_e32 v98, v100, v102
	v_mul_f32_e32 v96, v96, v110
	v_mul_f32_e32 v9, v101, v103
	v_mul_f32_e32 v11, v97, v105
	v_cvt_pk_fp8_f32 v12, v98, v9 op_sel:[0,0,1]
	v_cvt_pk_fp8_f32 v13, v96, v11 op_sel:[0,0,1]
	v_mad_i64_i32 v[94:95], s[26:27], v108, s73, v[4:5]
	v_lshl_add_u64 v[98:99], v[94:95], 0, v[6:7]
	global_store_dwordx2 v[106:107], v[12:13], off offset:128
	v_mov_b32_e32 v12, 0
	v_mov_b32_e32 v13, 0
	v_ashrrev_i32_e32 v109, 31, v108
	s_waitcnt vmcnt(15)
	v_mov_b32_e32 v94, v208
	v_mov_b32_e32 v95, v209
	v_mov_b32_e32 v96, v210
	v_mov_b32_e32 v97, v211
	v_lshlrev_b32_e32 v9, 16, v94
	v_and_b32_e32 v11, 0xffff0000, v94
	v_lshlrev_b32_e32 v100, 16, v96
	v_and_b32_e32 v96, 0xffff0000, v96
	v_mul_f32_e32 v9, 0xbfb8aa3b, v9
	v_mul_f32_e32 v100, 0xbfb8aa3b, v100
	v_mul_f32_e32 v11, 0xbfb8aa3b, v11
	v_mul_f32_e32 v96, 0xbfb8aa3b, v96
	v_exp_f32_e32 v9, v9
	v_exp_f32_e32 v100, v100
	v_exp_f32_e32 v11, v11
	v_exp_f32_e32 v96, v96
	v_lshlrev_b32_e32 v94, 16, v95
	v_and_b32_e32 v95, 0xffff0000, v95
	v_lshlrev_b32_e32 v101, 16, v97
	v_and_b32_e32 v97, 0xffff0000, v97
	v_mul_f32_e32 v94, 0xbfb8aa3b, v94
	v_mul_f32_e32 v101, 0xbfb8aa3b, v101
	v_mul_f32_e32 v95, 0xbfb8aa3b, v95
	v_mul_f32_e32 v97, 0xbfb8aa3b, v97
	v_exp_f32_e32 v94, v94
	v_exp_f32_e32 v101, v101
	v_exp_f32_e32 v95, v95
	v_exp_f32_e32 v97, v97
	v_add_f32_e32 v9, 1.0, v9
	v_add_f32_e32 v100, 1.0, v100
	v_add_f32_e32 v11, 1.0, v11
	v_add_f32_e32 v96, 1.0, v96
	v_rcp_f32_e32 v9, v9
	v_rcp_f32_e32 v100, v100
	v_rcp_f32_e32 v11, v11
	v_rcp_f32_e32 v96, v96
	v_add_f32_e32 v94, 1.0, v94
	v_add_f32_e32 v101, 1.0, v101
	v_add_f32_e32 v95, 1.0, v95
	v_add_f32_e32 v97, 1.0, v97
	v_rcp_f32_e32 v94, v94
	v_rcp_f32_e32 v101, v101
	v_rcp_f32_e32 v95, v95
	v_rcp_f32_e32 v97, v97
	v_mul_f32_e32 v9, 0x41800000, v9
	v_mul_f32_e32 v100, 0x41800000, v100
	v_mul_f32_e32 v11, 0x41800000, v11
	v_mul_f32_e32 v96, 0x41800000, v96
	v_mul_f32_e32 v9, v90, v9
	v_mul_f32_e32 v86, v86, v100
	v_mul_f32_e32 v11, v91, v11
	v_mul_f32_e32 v87, v87, v96
	v_cvt_pk_fp8_f32 v12, v9, v11
	v_cvt_pk_fp8_f32 v13, v86, v87
	v_mul_f32_e32 v94, 0x41800000, v94
	v_mul_f32_e32 v101, 0x41800000, v101
	v_mul_f32_e32 v95, 0x41800000, v95
	v_mul_f32_e32 v97, 0x41800000, v97
	v_mul_f32_e32 v90, v92, v94
	v_mul_f32_e32 v88, v88, v101
	v_mul_f32_e32 v9, v93, v95
	v_mul_f32_e32 v11, v89, v97
	v_cvt_pk_fp8_f32 v12, v90, v9 op_sel:[0,0,1]
	v_cvt_pk_fp8_f32 v13, v88, v11 op_sel:[0,0,1]
	v_lshlrev_b64 v[86:87], 11, v[108:109]
	v_lshl_add_u64 v[86:87], s[36:37], 0, v[86:87]
	v_lshl_add_u64 v[90:91], v[86:87], 0, v[2:3]
	global_store_dwordx2 v[90:91], v[12:13], off
	v_mov_b32_e32 v12, 0
	v_mov_b32_e32 v13, 0
	v_add_u32_e32 v92, 0x80, v8
	s_waitcnt vmcnt(15)
	v_mov_b32_e32 v86, v212
	v_mov_b32_e32 v87, v213
	v_mov_b32_e32 v88, v214
	v_mov_b32_e32 v89, v215
	v_lshlrev_b32_e32 v9, 16, v86
	v_and_b32_e32 v11, 0xffff0000, v86
	v_lshlrev_b32_e32 v93, 16, v88
	v_and_b32_e32 v88, 0xffff0000, v88
	v_mul_f32_e32 v9, 0xbfb8aa3b, v9
	v_mul_f32_e32 v93, 0xbfb8aa3b, v93
	v_mul_f32_e32 v11, 0xbfb8aa3b, v11
	v_mul_f32_e32 v88, 0xbfb8aa3b, v88
	v_exp_f32_e32 v9, v9
	v_exp_f32_e32 v93, v93
	v_exp_f32_e32 v11, v11
	v_exp_f32_e32 v88, v88
	v_lshlrev_b32_e32 v86, 16, v87
	v_and_b32_e32 v87, 0xffff0000, v87
	v_lshlrev_b32_e32 v94, 16, v89
	v_and_b32_e32 v89, 0xffff0000, v89
	v_mul_f32_e32 v86, 0xbfb8aa3b, v86
	v_mul_f32_e32 v94, 0xbfb8aa3b, v94
	v_mul_f32_e32 v87, 0xbfb8aa3b, v87
	v_mul_f32_e32 v89, 0xbfb8aa3b, v89
	v_exp_f32_e32 v86, v86
	v_exp_f32_e32 v94, v94
	v_exp_f32_e32 v87, v87
	v_exp_f32_e32 v89, v89
	v_add_f32_e32 v9, 1.0, v9
	v_add_f32_e32 v93, 1.0, v93
	v_add_f32_e32 v11, 1.0, v11
	v_add_f32_e32 v88, 1.0, v88
	v_rcp_f32_e32 v9, v9
	v_rcp_f32_e32 v93, v93
	v_rcp_f32_e32 v11, v11
	v_rcp_f32_e32 v88, v88
	v_add_f32_e32 v86, 1.0, v86
	v_add_f32_e32 v94, 1.0, v94
	v_add_f32_e32 v87, 1.0, v87
	v_add_f32_e32 v89, 1.0, v89
	v_rcp_f32_e32 v86, v86
	v_rcp_f32_e32 v94, v94
	v_rcp_f32_e32 v87, v87
	v_rcp_f32_e32 v89, v89
	v_mul_f32_e32 v9, 0x41800000, v9
	v_mul_f32_e32 v93, 0x41800000, v93
	v_mul_f32_e32 v11, 0x41800000, v11
	v_mul_f32_e32 v88, 0x41800000, v88
	v_mul_f32_e32 v9, v82, v9
	v_mul_f32_e32 v78, v78, v93
	v_mul_f32_e32 v11, v83, v11
	v_mul_f32_e32 v79, v79, v88
	v_cvt_pk_fp8_f32 v12, v9, v11
	v_cvt_pk_fp8_f32 v13, v78, v79
	v_mul_f32_e32 v86, 0x41800000, v86
	v_mul_f32_e32 v94, 0x41800000, v94
	v_mul_f32_e32 v87, 0x41800000, v87
	v_mul_f32_e32 v89, 0x41800000, v89
	v_mul_f32_e32 v82, v84, v86
	v_mul_f32_e32 v80, v80, v94
	v_mul_f32_e32 v9, v85, v87
	v_mul_f32_e32 v11, v81, v89
	v_cvt_pk_fp8_f32 v12, v82, v9 op_sel:[0,0,1]
	v_cvt_pk_fp8_f32 v13, v80, v11 op_sel:[0,0,1]
	v_mad_i64_i32 v[78:79], s[26:27], v92, s73, v[4:5]
	v_lshl_add_u64 v[82:83], v[78:79], 0, v[6:7]
	global_store_dwordx2 v[90:91], v[12:13], off offset:128
	v_mov_b32_e32 v12, 0
	v_mov_b32_e32 v13, 0
	v_ashrrev_i32_e32 v93, 31, v92
	s_waitcnt vmcnt(15)
; __device__ __forceinline__ unsigned cvt4_fp8(float a, float b, float c, float d) { int w = 0; w = __builtin_amdgcn_cvt_pk_fp8_f32(a, b, w, false); w = __builtin_amdgcn_cvt_pk_fp8_f32(c, d, w, true); return (unsigned)w; }
; __device__ __forceinline__ float sigmoidf_(float x) { return __builtin_amdgcn_rcpf(1.0f + __expf(-x)); }
; __device__ __forceinline__ void unpack8(u32x4 w, f32x4& a, f32x4& b) { a = (f32x4){bflo(w.x), bfhi(w.x), bflo(w.y), bfhi(w.y)}; b = (f32x4){bflo(w.z), bfhi(w.z), bflo(w.w), bfhi(w.w)}; }
;     __device__ __forceinline__ void operator()(const Acc& acc, const Unit& u, int wr, int wc, int fr, int fq) const {
;     ...
;                 for (int bj = 0; bj < 2; ++bj) { const int col = col0 + bj * HALF;
;                     f32x4 b0, b1; unpack8(*(const u32x4*)(GB + (size_t)row * ldg + col), b0, b1);
;                     f32x4 v0 = acc[ai][bj][m][0], v1 = acc[ai][bj][m][1];
; #pragma unroll
;                     for (int j = 0; j < 4; ++j) { v0[j] *= 16.0f * sigmoidf_(b0[j]); v1[j] *= 16.0f * sigmoidf_(b1[j]); }
;                     u32x2 w; w.x = cvt4_fp8(v0[0], v0[1], v0[2], v0[3]); w.y = cvt4_fp8(v1[0], v1[1], v1[2], v1[3]); *(u32x2*)(O + (size_t)row * ldc + col) = w; } }
	v_mov_b32_e32 v78, v216
	v_mov_b32_e32 v79, v217
	v_mov_b32_e32 v80, v218
	v_mov_b32_e32 v81, v219
	v_lshlrev_b32_e32 v9, 16, v78
	v_and_b32_e32 v11, 0xffff0000, v78
	v_lshlrev_b32_e32 v84, 16, v80
	v_and_b32_e32 v80, 0xffff0000, v80
	v_mul_f32_e32 v9, 0xbfb8aa3b, v9
	v_mul_f32_e32 v84, 0xbfb8aa3b, v84
	v_mul_f32_e32 v11, 0xbfb8aa3b, v11
	v_mul_f32_e32 v80, 0xbfb8aa3b, v80
	v_exp_f32_e32 v9, v9
	v_exp_f32_e32 v84, v84
	v_exp_f32_e32 v11, v11
	v_exp_f32_e32 v80, v80
	v_lshlrev_b32_e32 v78, 16, v79
	v_and_b32_e32 v79, 0xffff0000, v79
	v_lshlrev_b32_e32 v85, 16, v81
	v_and_b32_e32 v81, 0xffff0000, v81
	v_mul_f32_e32 v78, 0xbfb8aa3b, v78
	v_mul_f32_e32 v85, 0xbfb8aa3b, v85
	v_mul_f32_e32 v79, 0xbfb8aa3b, v79
	v_mul_f32_e32 v81, 0xbfb8aa3b, v81
	v_exp_f32_e32 v78, v78
	v_exp_f32_e32 v85, v85
	v_exp_f32_e32 v79, v79
	v_exp_f32_e32 v81, v81
	v_add_f32_e32 v9, 1.0, v9
	v_add_f32_e32 v84, 1.0, v84
	v_add_f32_e32 v11, 1.0, v11
	v_add_f32_e32 v80, 1.0, v80
	v_rcp_f32_e32 v9, v9
	v_rcp_f32_e32 v84, v84
	v_rcp_f32_e32 v11, v11
	v_rcp_f32_e32 v80, v80
	v_add_f32_e32 v78, 1.0, v78
	v_add_f32_e32 v85, 1.0, v85
	v_add_f32_e32 v79, 1.0, v79
	v_add_f32_e32 v81, 1.0, v81
	v_rcp_f32_e32 v78, v78
	v_rcp_f32_e32 v85, v85
	v_rcp_f32_e32 v79, v79
	v_rcp_f32_e32 v81, v81
	v_mul_f32_e32 v9, 0x41800000, v9
	v_mul_f32_e32 v84, 0x41800000, v84
	v_mul_f32_e32 v11, 0x41800000, v11
	v_mul_f32_e32 v80, 0x41800000, v80
	v_mul_f32_e32 v9, v74, v9
	v_mul_f32_e32 v70, v70, v84
	v_mul_f32_e32 v11, v75, v11
	v_mul_f32_e32 v71, v71, v80
	v_cvt_pk_fp8_f32 v12, v9, v11
	v_cvt_pk_fp8_f32 v13, v70, v71
	v_mul_f32_e32 v78, 0x41800000, v78
	v_mul_f32_e32 v85, 0x41800000, v85
	v_mul_f32_e32 v79, 0x41800000, v79
	v_mul_f32_e32 v81, 0x41800000, v81
	v_mul_f32_e32 v74, v76, v78
	v_mul_f32_e32 v72, v72, v85
	v_mul_f32_e32 v9, v77, v79
	v_mul_f32_e32 v11, v73, v81
	v_cvt_pk_fp8_f32 v12, v74, v9 op_sel:[0,0,1]
	v_cvt_pk_fp8_f32 v13, v72, v11 op_sel:[0,0,1]
	v_lshlrev_b64 v[70:71], 11, v[92:93]
	v_lshl_add_u64 v[70:71], s[36:37], 0, v[70:71]
	v_lshl_add_u64 v[74:75], v[70:71], 0, v[2:3]
	global_store_dwordx2 v[74:75], v[12:13], off
	v_mov_b32_e32 v12, 0
	v_mov_b32_e32 v13, 0
	v_add_u32_e32 v76, 0x90, v8
	s_waitcnt vmcnt(15)
	v_mov_b32_e32 v70, v220
	v_mov_b32_e32 v71, v221
	v_mov_b32_e32 v72, v222
	v_mov_b32_e32 v73, v223
	v_lshlrev_b32_e32 v9, 16, v70
	v_and_b32_e32 v11, 0xffff0000, v70
	v_lshlrev_b32_e32 v77, 16, v72
	v_and_b32_e32 v72, 0xffff0000, v72
	v_mul_f32_e32 v9, 0xbfb8aa3b, v9
	v_mul_f32_e32 v77, 0xbfb8aa3b, v77
	v_mul_f32_e32 v11, 0xbfb8aa3b, v11
	v_mul_f32_e32 v72, 0xbfb8aa3b, v72
	v_exp_f32_e32 v9, v9
	v_exp_f32_e32 v77, v77
	v_exp_f32_e32 v11, v11
	v_exp_f32_e32 v72, v72
	v_lshlrev_b32_e32 v70, 16, v71
	v_and_b32_e32 v71, 0xffff0000, v71
	v_lshlrev_b32_e32 v78, 16, v73
	v_and_b32_e32 v73, 0xffff0000, v73
	v_mul_f32_e32 v70, 0xbfb8aa3b, v70
	v_mul_f32_e32 v78, 0xbfb8aa3b, v78
	v_mul_f32_e32 v71, 0xbfb8aa3b, v71
	v_mul_f32_e32 v73, 0xbfb8aa3b, v73
	v_exp_f32_e32 v70, v70
	v_exp_f32_e32 v78, v78
	v_exp_f32_e32 v71, v71
	v_exp_f32_e32 v73, v73
	v_add_f32_e32 v9, 1.0, v9
	v_add_f32_e32 v77, 1.0, v77
	v_add_f32_e32 v11, 1.0, v11
	v_add_f32_e32 v72, 1.0, v72
	v_rcp_f32_e32 v9, v9
	v_rcp_f32_e32 v77, v77
	v_rcp_f32_e32 v11, v11
	v_rcp_f32_e32 v72, v72
	v_add_f32_e32 v70, 1.0, v70
	v_add_f32_e32 v78, 1.0, v78
	v_add_f32_e32 v71, 1.0, v71
	v_add_f32_e32 v73, 1.0, v73
	v_rcp_f32_e32 v70, v70
	v_rcp_f32_e32 v78, v78
	v_rcp_f32_e32 v71, v71
	v_rcp_f32_e32 v73, v73
	v_mul_f32_e32 v9, 0x41800000, v9
	v_mul_f32_e32 v77, 0x41800000, v77
	v_mul_f32_e32 v11, 0x41800000, v11
	v_mul_f32_e32 v72, 0x41800000, v72
	v_mul_f32_e32 v9, v66, v9
	v_mul_f32_e32 v62, v62, v77
	v_mul_f32_e32 v11, v67, v11
	v_mul_f32_e32 v63, v63, v72
	v_cvt_pk_fp8_f32 v12, v9, v11
	v_cvt_pk_fp8_f32 v13, v62, v63
	v_mul_f32_e32 v70, 0x41800000, v70
	v_mul_f32_e32 v78, 0x41800000, v78
	v_mul_f32_e32 v71, 0x41800000, v71
	v_mul_f32_e32 v73, 0x41800000, v73
	v_mul_f32_e32 v66, v68, v70
	v_mul_f32_e32 v64, v64, v78
	v_mul_f32_e32 v9, v69, v71
	v_mul_f32_e32 v11, v65, v73
	v_cvt_pk_fp8_f32 v12, v66, v9 op_sel:[0,0,1]
	v_cvt_pk_fp8_f32 v13, v64, v11 op_sel:[0,0,1]
	v_mad_i64_i32 v[62:63], s[26:27], v76, s73, v[4:5]
	v_lshl_add_u64 v[66:67], v[62:63], 0, v[6:7]
	global_store_dwordx2 v[74:75], v[12:13], off offset:128
	v_mov_b32_e32 v12, 0
	v_mov_b32_e32 v13, 0
	v_ashrrev_i32_e32 v77, 31, v76
	s_waitcnt vmcnt(15)
	v_mov_b32_e32 v62, v224
	v_mov_b32_e32 v63, v225
	v_mov_b32_e32 v64, v226
	v_mov_b32_e32 v65, v227
	v_lshlrev_b32_e32 v9, 16, v62
	v_and_b32_e32 v11, 0xffff0000, v62
	v_lshlrev_b32_e32 v68, 16, v64
	v_and_b32_e32 v64, 0xffff0000, v64
	v_mul_f32_e32 v9, 0xbfb8aa3b, v9
	v_mul_f32_e32 v68, 0xbfb8aa3b, v68
	v_mul_f32_e32 v11, 0xbfb8aa3b, v11
	v_mul_f32_e32 v64, 0xbfb8aa3b, v64
	v_exp_f32_e32 v9, v9
	v_exp_f32_e32 v68, v68
	v_exp_f32_e32 v11, v11
	v_exp_f32_e32 v64, v64
	v_lshlrev_b32_e32 v62, 16, v63
	v_and_b32_e32 v63, 0xffff0000, v63
	v_lshlrev_b32_e32 v69, 16, v65
	v_and_b32_e32 v65, 0xffff0000, v65
	v_mul_f32_e32 v62, 0xbfb8aa3b, v62
	v_mul_f32_e32 v69, 0xbfb8aa3b, v69
	v_mul_f32_e32 v63, 0xbfb8aa3b, v63
	v_mul_f32_e32 v65, 0xbfb8aa3b, v65
	v_exp_f32_e32 v62, v62
	v_exp_f32_e32 v69, v69
	v_exp_f32_e32 v63, v63
	v_exp_f32_e32 v65, v65
	v_add_f32_e32 v9, 1.0, v9
	v_add_f32_e32 v68, 1.0, v68
	v_add_f32_e32 v11, 1.0, v11
	v_add_f32_e32 v64, 1.0, v64
	v_rcp_f32_e32 v9, v9
	v_rcp_f32_e32 v68, v68
	v_rcp_f32_e32 v11, v11
	v_rcp_f32_e32 v64, v64
	v_add_f32_e32 v62, 1.0, v62
	v_add_f32_e32 v69, 1.0, v69
	v_add_f32_e32 v63, 1.0, v63
	v_add_f32_e32 v65, 1.0, v65
	v_rcp_f32_e32 v62, v62
	v_rcp_f32_e32 v69, v69
	v_rcp_f32_e32 v63, v63
	v_rcp_f32_e32 v65, v65
	v_mul_f32_e32 v9, 0x41800000, v9
	v_mul_f32_e32 v68, 0x41800000, v68
	v_mul_f32_e32 v11, 0x41800000, v11
	v_mul_f32_e32 v64, 0x41800000, v64
	v_mul_f32_e32 v9, v58, v9
	v_mul_f32_e32 v54, v54, v68
	v_mul_f32_e32 v11, v59, v11
	v_mul_f32_e32 v55, v55, v64
	v_cvt_pk_fp8_f32 v12, v9, v11
	v_cvt_pk_fp8_f32 v13, v54, v55
	v_mul_f32_e32 v62, 0x41800000, v62
	v_mul_f32_e32 v69, 0x41800000, v69
	v_mul_f32_e32 v63, 0x41800000, v63
	v_mul_f32_e32 v65, 0x41800000, v65
	v_mul_f32_e32 v58, v60, v62
	v_mul_f32_e32 v56, v56, v69
	v_mul_f32_e32 v9, v61, v63
	v_mul_f32_e32 v11, v57, v65
	v_cvt_pk_fp8_f32 v12, v58, v9 op_sel:[0,0,1]
	v_cvt_pk_fp8_f32 v13, v56, v11 op_sel:[0,0,1]
	v_lshlrev_b64 v[54:55], 11, v[76:77]
	v_lshl_add_u64 v[54:55], s[36:37], 0, v[54:55]
	v_lshl_add_u64 v[58:59], v[54:55], 0, v[2:3]
	global_store_dwordx2 v[58:59], v[12:13], off
	v_mov_b32_e32 v12, 0
	v_mov_b32_e32 v13, 0
	v_add_u32_e32 v60, 0xa0, v8
	v_add_u32_e32 v8, 0xb0, v8
	s_waitcnt vmcnt(15)
; __device__ __forceinline__ unsigned cvt4_fp8(float a, float b, float c, float d) { int w = 0; w = __builtin_amdgcn_cvt_pk_fp8_f32(a, b, w, false); w = __builtin_amdgcn_cvt_pk_fp8_f32(c, d, w, true); return (unsigned)w; }
; __device__ __forceinline__ float sigmoidf_(float x) { return __builtin_amdgcn_rcpf(1.0f + __expf(-x)); }
; __device__ __forceinline__ void unpack8(u32x4 w, f32x4& a, f32x4& b) { a = (f32x4){bflo(w.x), bfhi(w.x), bflo(w.y), bfhi(w.y)}; b = (f32x4){bflo(w.z), bfhi(w.z), bflo(w.w), bfhi(w.w)}; }
;     __device__ __forceinline__ void operator()(const Acc& acc, const Unit& u, int wr, int wc, int fr, int fq) const {
;     ...
;                 for (int bj = 0; bj < 2; ++bj) { const int col = col0 + bj * HALF;
;                     f32x4 b0, b1; unpack8(*(const u32x4*)(GB + (size_t)row * ldg + col), b0, b1);
;                     f32x4 v0 = acc[ai][bj][m][0], v1 = acc[ai][bj][m][1];
; #pragma unroll
;                     for (int j = 0; j < 4; ++j) { v0[j] *= 16.0f * sigmoidf_(b0[j]); v1[j] *= 16.0f * sigmoidf_(b1[j]); }
;                     u32x2 w; w.x = cvt4_fp8(v0[0], v0[1], v0[2], v0[3]); w.y = cvt4_fp8(v1[0], v1[1], v1[2], v1[3]); *(u32x2*)(O + (size_t)row * ldc + col) = w; } }
	v_mov_b32_e32 v54, v228
	v_mov_b32_e32 v55, v229
	v_mov_b32_e32 v56, v230
	v_mov_b32_e32 v57, v231
	v_lshlrev_b32_e32 v9, 16, v54
	v_and_b32_e32 v11, 0xffff0000, v54
	v_lshlrev_b32_e32 v61, 16, v56
	v_and_b32_e32 v56, 0xffff0000, v56
	v_mul_f32_e32 v9, 0xbfb8aa3b, v9
	v_mul_f32_e32 v61, 0xbfb8aa3b, v61
	v_mul_f32_e32 v11, 0xbfb8aa3b, v11
	v_mul_f32_e32 v56, 0xbfb8aa3b, v56
	v_exp_f32_e32 v9, v9
	v_exp_f32_e32 v61, v61
	v_exp_f32_e32 v11, v11
	v_exp_f32_e32 v56, v56
	v_lshlrev_b32_e32 v54, 16, v55
	v_and_b32_e32 v55, 0xffff0000, v55
	v_lshlrev_b32_e32 v62, 16, v57
	v_and_b32_e32 v57, 0xffff0000, v57
	v_mul_f32_e32 v54, 0xbfb8aa3b, v54
	v_mul_f32_e32 v62, 0xbfb8aa3b, v62
	v_mul_f32_e32 v55, 0xbfb8aa3b, v55
	v_mul_f32_e32 v57, 0xbfb8aa3b, v57
	v_exp_f32_e32 v54, v54
	v_exp_f32_e32 v62, v62
	v_exp_f32_e32 v55, v55
	v_exp_f32_e32 v57, v57
	v_add_f32_e32 v9, 1.0, v9
	v_add_f32_e32 v61, 1.0, v61
	v_add_f32_e32 v11, 1.0, v11
	v_add_f32_e32 v56, 1.0, v56
	v_rcp_f32_e32 v9, v9
	v_rcp_f32_e32 v61, v61
	v_rcp_f32_e32 v11, v11
	v_rcp_f32_e32 v56, v56
	v_add_f32_e32 v54, 1.0, v54
	v_add_f32_e32 v62, 1.0, v62
	v_add_f32_e32 v55, 1.0, v55
	v_add_f32_e32 v57, 1.0, v57
	v_rcp_f32_e32 v54, v54
	v_rcp_f32_e32 v62, v62
	v_rcp_f32_e32 v55, v55
	v_rcp_f32_e32 v57, v57
	v_mul_f32_e32 v9, 0x41800000, v9
	v_mul_f32_e32 v61, 0x41800000, v61
	v_mul_f32_e32 v11, 0x41800000, v11
	v_mul_f32_e32 v56, 0x41800000, v56
	v_mul_f32_e32 v9, v50, v9
	v_mul_f32_e32 v46, v46, v61
	v_mul_f32_e32 v11, v51, v11
	v_mul_f32_e32 v47, v47, v56
	v_cvt_pk_fp8_f32 v12, v9, v11
	v_cvt_pk_fp8_f32 v13, v46, v47
	v_mul_f32_e32 v54, 0x41800000, v54
	v_mul_f32_e32 v62, 0x41800000, v62
	v_mul_f32_e32 v55, 0x41800000, v55
	v_mul_f32_e32 v57, 0x41800000, v57
	v_mul_f32_e32 v50, v52, v54
	v_mul_f32_e32 v48, v48, v62
	v_mul_f32_e32 v9, v53, v55
	v_mul_f32_e32 v11, v49, v57
	v_cvt_pk_fp8_f32 v12, v50, v9 op_sel:[0,0,1]
	v_cvt_pk_fp8_f32 v13, v48, v11 op_sel:[0,0,1]
	v_mad_i64_i32 v[46:47], s[26:27], v60, s73, v[4:5]
	v_lshl_add_u64 v[50:51], v[46:47], 0, v[6:7]
	global_store_dwordx2 v[58:59], v[12:13], off offset:128
	v_mov_b32_e32 v12, 0
	v_mov_b32_e32 v13, 0
	v_ashrrev_i32_e32 v61, 31, v60
	v_mad_i64_i32 v[4:5], s[26:27], v8, s73, v[4:5]
	s_waitcnt vmcnt(15)
	v_mov_b32_e32 v46, v232
	v_mov_b32_e32 v47, v233
	v_mov_b32_e32 v48, v234
	v_mov_b32_e32 v49, v235
	v_lshlrev_b32_e32 v9, 16, v46
	v_and_b32_e32 v11, 0xffff0000, v46
	v_lshlrev_b32_e32 v52, 16, v48
	v_and_b32_e32 v48, 0xffff0000, v48
	v_mul_f32_e32 v9, 0xbfb8aa3b, v9
	v_mul_f32_e32 v52, 0xbfb8aa3b, v52
	v_mul_f32_e32 v11, 0xbfb8aa3b, v11
	v_mul_f32_e32 v48, 0xbfb8aa3b, v48
	v_exp_f32_e32 v9, v9
	v_exp_f32_e32 v52, v52
	v_exp_f32_e32 v11, v11
	v_exp_f32_e32 v48, v48
	v_lshlrev_b32_e32 v46, 16, v47
	v_and_b32_e32 v47, 0xffff0000, v47
	v_lshlrev_b32_e32 v53, 16, v49
	v_and_b32_e32 v49, 0xffff0000, v49
	v_mul_f32_e32 v46, 0xbfb8aa3b, v46
	v_mul_f32_e32 v53, 0xbfb8aa3b, v53
	v_mul_f32_e32 v47, 0xbfb8aa3b, v47
	v_mul_f32_e32 v49, 0xbfb8aa3b, v49
	v_exp_f32_e32 v46, v46
	v_exp_f32_e32 v53, v53
	v_exp_f32_e32 v47, v47
	v_exp_f32_e32 v49, v49
	v_add_f32_e32 v9, 1.0, v9
	v_add_f32_e32 v52, 1.0, v52
	v_add_f32_e32 v11, 1.0, v11
	v_add_f32_e32 v48, 1.0, v48
	v_rcp_f32_e32 v9, v9
	v_rcp_f32_e32 v52, v52
	v_rcp_f32_e32 v11, v11
	v_rcp_f32_e32 v48, v48
	v_add_f32_e32 v46, 1.0, v46
	v_add_f32_e32 v53, 1.0, v53
	v_add_f32_e32 v47, 1.0, v47
	v_add_f32_e32 v49, 1.0, v49
	v_rcp_f32_e32 v46, v46
	v_rcp_f32_e32 v53, v53
	v_rcp_f32_e32 v47, v47
	v_rcp_f32_e32 v49, v49
	v_mul_f32_e32 v9, 0x41800000, v9
	v_mul_f32_e32 v52, 0x41800000, v52
	v_mul_f32_e32 v11, 0x41800000, v11
	v_mul_f32_e32 v48, 0x41800000, v48
	v_mul_f32_e32 v9, v42, v9
	v_mul_f32_e32 v38, v38, v52
	v_mul_f32_e32 v11, v43, v11
	v_mul_f32_e32 v39, v39, v48
	v_cvt_pk_fp8_f32 v12, v9, v11
	v_cvt_pk_fp8_f32 v13, v38, v39
	v_mul_f32_e32 v46, 0x41800000, v46
	v_mul_f32_e32 v53, 0x41800000, v53
	v_mul_f32_e32 v47, 0x41800000, v47
	v_mul_f32_e32 v49, 0x41800000, v49
	v_mul_f32_e32 v42, v44, v46
	v_mul_f32_e32 v40, v40, v53
	v_mul_f32_e32 v9, v45, v47
	v_mul_f32_e32 v11, v41, v49
	v_cvt_pk_fp8_f32 v12, v42, v9 op_sel:[0,0,1]
	v_cvt_pk_fp8_f32 v13, v40, v11 op_sel:[0,0,1]
	v_lshlrev_b64 v[38:39], 11, v[60:61]
	v_lshl_add_u64 v[38:39], s[36:37], 0, v[38:39]
	v_lshl_add_u64 v[42:43], v[38:39], 0, v[2:3]
	global_store_dwordx2 v[42:43], v[12:13], off
	v_mov_b32_e32 v12, 0
	v_mov_b32_e32 v13, 0
	s_waitcnt vmcnt(15)
; __device__ __forceinline__ unsigned cvt4_fp8(float a, float b, float c, float d) { int w = 0; w = __builtin_amdgcn_cvt_pk_fp8_f32(a, b, w, false); w = __builtin_amdgcn_cvt_pk_fp8_f32(c, d, w, true); return (unsigned)w; }
; __device__ __forceinline__ float sigmoidf_(float x) { return __builtin_amdgcn_rcpf(1.0f + __expf(-x)); }
; __device__ __forceinline__ void unpack8(u32x4 w, f32x4& a, f32x4& b) { a = (f32x4){bflo(w.x), bfhi(w.x), bflo(w.y), bfhi(w.y)}; b = (f32x4){bflo(w.z), bfhi(w.z), bflo(w.w), bfhi(w.w)}; }
;     __device__ __forceinline__ void operator()(const Acc& acc, const Unit& u, int wr, int wc, int fr, int fq) const {
;     ...
;                 for (int bj = 0; bj < 2; ++bj) { const int col = col0 + bj * HALF;
;                     f32x4 b0, b1; unpack8(*(const u32x4*)(GB + (size_t)row * ldg + col), b0, b1);
;                     f32x4 v0 = acc[ai][bj][m][0], v1 = acc[ai][bj][m][1];
; #pragma unroll
;                     for (int j = 0; j < 4; ++j) { v0[j] *= 16.0f * sigmoidf_(b0[j]); v1[j] *= 16.0f * sigmoidf_(b1[j]); }
;                     u32x2 w; w.x = cvt4_fp8(v0[0], v0[1], v0[2], v0[3]); w.y = cvt4_fp8(v1[0], v1[1], v1[2], v1[3]); *(u32x2*)(O + (size_t)row * ldc + col) = w; } }
;     }
	v_mov_b32_e32 v38, v236
	v_mov_b32_e32 v39, v237
	v_mov_b32_e32 v40, v238
	v_mov_b32_e32 v41, v239
	v_lshlrev_b32_e32 v9, 16, v38
	v_and_b32_e32 v11, 0xffff0000, v38
	v_lshlrev_b32_e32 v44, 16, v40
	v_and_b32_e32 v40, 0xffff0000, v40
	v_mul_f32_e32 v9, 0xbfb8aa3b, v9
	v_mul_f32_e32 v44, 0xbfb8aa3b, v44
	v_mul_f32_e32 v11, 0xbfb8aa3b, v11
	v_mul_f32_e32 v40, 0xbfb8aa3b, v40
	v_exp_f32_e32 v9, v9
	v_exp_f32_e32 v44, v44
	v_exp_f32_e32 v11, v11
	v_exp_f32_e32 v40, v40
	v_lshlrev_b32_e32 v38, 16, v39
	v_and_b32_e32 v39, 0xffff0000, v39
	v_lshlrev_b32_e32 v45, 16, v41
	v_and_b32_e32 v41, 0xffff0000, v41
	v_mul_f32_e32 v38, 0xbfb8aa3b, v38
	v_mul_f32_e32 v45, 0xbfb8aa3b, v45
	v_mul_f32_e32 v39, 0xbfb8aa3b, v39
	v_mul_f32_e32 v41, 0xbfb8aa3b, v41
	v_exp_f32_e32 v38, v38
	v_exp_f32_e32 v45, v45
	v_exp_f32_e32 v39, v39
	v_exp_f32_e32 v41, v41
	v_add_f32_e32 v9, 1.0, v9
	v_add_f32_e32 v44, 1.0, v44
	v_add_f32_e32 v11, 1.0, v11
	v_add_f32_e32 v40, 1.0, v40
	v_rcp_f32_e32 v9, v9
	v_rcp_f32_e32 v44, v44
	v_rcp_f32_e32 v11, v11
	v_rcp_f32_e32 v40, v40
	v_add_f32_e32 v38, 1.0, v38
	v_add_f32_e32 v45, 1.0, v45
	v_add_f32_e32 v39, 1.0, v39
	v_add_f32_e32 v41, 1.0, v41
	v_rcp_f32_e32 v38, v38
	v_rcp_f32_e32 v45, v45
	v_rcp_f32_e32 v39, v39
	v_rcp_f32_e32 v41, v41
	v_mul_f32_e32 v9, 0x41800000, v9
	v_mul_f32_e32 v44, 0x41800000, v44
	v_mul_f32_e32 v11, 0x41800000, v11
	v_mul_f32_e32 v40, 0x41800000, v40
	v_mul_f32_e32 v9, v30, v9
	v_mul_f32_e32 v30, v34, v44
	v_mul_f32_e32 v11, v31, v11
	v_mul_f32_e32 v31, v35, v40
	v_cvt_pk_fp8_f32 v12, v9, v11
	v_cvt_pk_fp8_f32 v13, v30, v31
	v_mul_f32_e32 v38, 0x41800000, v38
	v_mul_f32_e32 v45, 0x41800000, v45
	v_mul_f32_e32 v39, 0x41800000, v39
	v_mul_f32_e32 v41, 0x41800000, v41
	v_mul_f32_e32 v32, v32, v38
	v_mul_f32_e32 v34, v36, v45
	v_mul_f32_e32 v9, v33, v39
	v_mul_f32_e32 v11, v37, v41
	v_cvt_pk_fp8_f32 v12, v32, v9 op_sel:[0,0,1]
	v_cvt_pk_fp8_f32 v13, v34, v11 op_sel:[0,0,1]
	v_lshl_add_u64 v[30:31], v[4:5], 0, v[6:7]
	v_ashrrev_i32_e32 v9, 31, v8
	global_store_dwordx2 v[42:43], v[12:13], off offset:128
	v_mov_b32_e32 v12, 0
	v_mov_b32_e32 v13, 0
	s_waitcnt vmcnt(15)
	v_mov_b32_e32 v4, v240
	v_mov_b32_e32 v5, v241
	v_mov_b32_e32 v6, v242
	v_mov_b32_e32 v7, v243
	v_lshlrev_b32_e32 v11, 16, v4
	v_and_b32_e32 v4, 0xffff0000, v4
	v_lshlrev_b32_e32 v33, 16, v6
	v_and_b32_e32 v6, 0xffff0000, v6
	v_mul_f32_e32 v11, 0xbfb8aa3b, v11
	v_mul_f32_e32 v33, 0xbfb8aa3b, v33
	v_mul_f32_e32 v4, 0xbfb8aa3b, v4
	v_mul_f32_e32 v6, 0xbfb8aa3b, v6
	v_exp_f32_e32 v11, v11
	v_exp_f32_e32 v33, v33
	v_exp_f32_e32 v4, v4
	v_exp_f32_e32 v6, v6
	v_lshlrev_b32_e32 v32, 16, v5
	v_and_b32_e32 v5, 0xffff0000, v5
	v_lshlrev_b32_e32 v34, 16, v7
	v_and_b32_e32 v7, 0xffff0000, v7
	v_mul_f32_e32 v32, 0xbfb8aa3b, v32
	v_mul_f32_e32 v34, 0xbfb8aa3b, v34
	v_mul_f32_e32 v5, 0xbfb8aa3b, v5
	v_mul_f32_e32 v7, 0xbfb8aa3b, v7
	v_exp_f32_e32 v32, v32
	v_exp_f32_e32 v34, v34
	v_exp_f32_e32 v5, v5
	v_exp_f32_e32 v7, v7
	v_add_f32_e32 v11, 1.0, v11
	v_add_f32_e32 v33, 1.0, v33
	v_add_f32_e32 v4, 1.0, v4
	v_add_f32_e32 v6, 1.0, v6
	v_rcp_f32_e32 v11, v11
	v_rcp_f32_e32 v33, v33
	v_rcp_f32_e32 v4, v4
	v_rcp_f32_e32 v6, v6
	v_add_f32_e32 v32, 1.0, v32
	v_add_f32_e32 v34, 1.0, v34
	v_add_f32_e32 v5, 1.0, v5
	v_add_f32_e32 v7, 1.0, v7
	v_rcp_f32_e32 v32, v32
	v_rcp_f32_e32 v34, v34
	v_rcp_f32_e32 v5, v5
	v_rcp_f32_e32 v7, v7
	v_mul_f32_e32 v11, 0x41800000, v11
	v_mul_f32_e32 v33, 0x41800000, v33
	v_mul_f32_e32 v4, 0x41800000, v4
	v_mul_f32_e32 v6, 0x41800000, v6
	v_mul_f32_e32 v11, v26, v11
	v_mul_f32_e32 v22, v22, v33
	v_mul_f32_e32 v4, v27, v4
	v_mul_f32_e32 v6, v23, v6
	v_cvt_pk_fp8_f32 v12, v11, v4
	v_cvt_pk_fp8_f32 v13, v22, v6
	v_mul_f32_e32 v32, 0x41800000, v32
	v_mul_f32_e32 v34, 0x41800000, v34
	v_mul_f32_e32 v5, 0x41800000, v5
	v_mul_f32_e32 v7, 0x41800000, v7
	v_mul_f32_e32 v23, v28, v32
	v_mul_f32_e32 v24, v24, v34
	v_mul_f32_e32 v4, v29, v5
	v_mul_f32_e32 v5, v25, v7
	v_cvt_pk_fp8_f32 v12, v23, v4 op_sel:[0,0,1]
	v_cvt_pk_fp8_f32 v13, v24, v5 op_sel:[0,0,1]
	v_lshlrev_b64 v[4:5], 11, v[8:9]
	v_lshl_add_u64 v[4:5], s[36:37], 0, v[4:5]
	v_lshl_add_u64 v[6:7], v[4:5], 0, v[2:3]
	global_store_dwordx2 v[6:7], v[12:13], off
	v_mov_b32_e32 v8, 0
	v_mov_b32_e32 v9, 0
	s_waitcnt vmcnt(15)
	v_mov_b32_e32 v2, v244
	v_mov_b32_e32 v3, v245
	v_mov_b32_e32 v4, v246
	v_mov_b32_e32 v5, v247
	v_lshlrev_b32_e32 v11, 16, v2
	v_and_b32_e32 v2, 0xffff0000, v2
	v_lshlrev_b32_e32 v13, 16, v4
	v_and_b32_e32 v4, 0xffff0000, v4
	v_mul_f32_e32 v11, 0xbfb8aa3b, v11
	v_mul_f32_e32 v13, 0xbfb8aa3b, v13
	v_mul_f32_e32 v2, 0xbfb8aa3b, v2
	v_mul_f32_e32 v4, 0xbfb8aa3b, v4
	v_exp_f32_e32 v11, v11
	v_exp_f32_e32 v13, v13
	v_exp_f32_e32 v2, v2
	v_exp_f32_e32 v4, v4
	v_lshlrev_b32_e32 v12, 16, v3
	v_and_b32_e32 v3, 0xffff0000, v3
	v_lshlrev_b32_e32 v22, 16, v5
	v_and_b32_e32 v5, 0xffff0000, v5
	v_mul_f32_e32 v12, 0xbfb8aa3b, v12
	v_mul_f32_e32 v22, 0xbfb8aa3b, v22
	v_mul_f32_e32 v3, 0xbfb8aa3b, v3
	v_mul_f32_e32 v5, 0xbfb8aa3b, v5
	v_exp_f32_e32 v12, v12
	v_exp_f32_e32 v22, v22
	v_exp_f32_e32 v3, v3
	v_exp_f32_e32 v5, v5
	v_add_f32_e32 v11, 1.0, v11
	v_add_f32_e32 v13, 1.0, v13
	v_add_f32_e32 v2, 1.0, v2
	v_add_f32_e32 v4, 1.0, v4
	v_rcp_f32_e32 v11, v11
	v_rcp_f32_e32 v13, v13
	v_rcp_f32_e32 v2, v2
	v_rcp_f32_e32 v4, v4
	v_add_f32_e32 v12, 1.0, v12
	v_add_f32_e32 v22, 1.0, v22
	v_add_f32_e32 v3, 1.0, v3
	v_add_f32_e32 v5, 1.0, v5
	v_rcp_f32_e32 v12, v12
	v_rcp_f32_e32 v22, v22
	v_rcp_f32_e32 v3, v3
	v_rcp_f32_e32 v5, v5
	v_mul_f32_e32 v11, 0x41800000, v11
	v_mul_f32_e32 v13, 0x41800000, v13
	v_mul_f32_e32 v2, 0x41800000, v2
	v_mul_f32_e32 v4, 0x41800000, v4
	v_mul_f32_e32 v11, v14, v11
	v_mul_f32_e32 v13, v18, v13
	v_mul_f32_e32 v2, v15, v2
	v_mul_f32_e32 v4, v19, v4
	v_cvt_pk_fp8_f32 v8, v11, v2
	v_cvt_pk_fp8_f32 v9, v13, v4
	v_mul_f32_e32 v12, 0x41800000, v12
	v_mul_f32_e32 v22, 0x41800000, v22
	v_mul_f32_e32 v3, 0x41800000, v3
	v_mul_f32_e32 v5, 0x41800000, v5
	v_mul_f32_e32 v12, v16, v12
	v_mul_f32_e32 v14, v20, v22
	v_mul_f32_e32 v2, v17, v3
	v_mul_f32_e32 v3, v21, v5
	v_cvt_pk_fp8_f32 v8, v12, v2 op_sel:[0,0,1]
	v_cvt_pk_fp8_f32 v9, v14, v3 op_sel:[0,0,1]
	global_store_dwordx2 v[6:7], v[8:9], off offset:128
	s_cbranch_vccnz .LBB0_1842
	s_andn2_b64 vcc, exec, s[4:5]
	s_cbranch_vccnz .LBB0_1841
	s_barrier
	s_branch .LBB0_1841
